# attention main loop: packed f32 fma/add among the MFMAs split into scalar pairs (cost-weighted spacing lever 7.5)
# baseline (speedup 1.0000x reference)
.LBB0_251:
	.p2align 3
	s_nop 0
	s_add_u32 s72, s90, s70
	s_addc_u32 s73, s91, s71
	s_add_u32 s6, s72, 0x100000
	s_addc_u32 s7, s73, 0
	s_add_u32 s88, s92, s70
	s_addc_u32 s89, s93, s71
	s_mov_b32 m0, s85
	s_nop 0
	global_load_lds_dwordx4 v168, s[6:7] offset:0
	s_add_u32 s6, s88, 0x100000
	s_addc_u32 s7, s89, 0
	s_mov_b32 m0, s86
	s_nop 0
	global_load_lds_dwordx4 v169, s[6:7] offset:0
	s_nop 0
	s_mov_b32 m0, s87
	s_nop 0
	global_load_lds_dwordx4 v170, s[6:7] offset:0
	ds_read_b128 v[66:69], v175
	ds_read_b128 v[82:85], v175 offset:4096
	ds_read_b128 v[114:117], v176
	ds_read_b128 v[184:187], v176 offset:4096
	ds_read_b128 v[196:199], v177
	ds_read_b128 v[200:203], v177 offset:4096
	ds_read_b128 v[204:207], v178
	ds_read_b128 v[208:211], v178 offset:4096
	s_waitcnt lgkmcnt(7)
	v_mfma_f32_32x32x16_bf16 v[66:81], v[66:69], v[110:113], 0
	v_exp_f32_e32 v120, v154
	v_exp_f32_e32 v121, v155
	v_exp_f32_e32 v152, v152
	v_exp_f32_e32 v153, v153
	v_exp_f32_e32 v150, v150
	v_exp_f32_e32 v151, v151
	v_exp_f32_e32 v148, v148
	s_waitcnt lgkmcnt(6)
	v_mfma_f32_32x32x16_bf16 v[82:97], v[82:85], v[110:113], 0
	v_exp_f32_e32 v149, v149
	v_exp_f32_e32 v146, v146
	v_exp_f32_e32 v147, v147
	v_exp_f32_e32 v144, v144
	v_exp_f32_e32 v145, v145
	v_exp_f32_e32 v154, v140
	v_exp_f32_e32 v155, v141
	s_waitcnt lgkmcnt(5)
	v_mfma_f32_32x32x16_bf16 v[66:81], v[114:117], v[106:109], v[66:81]
	v_exp_f32_e32 v116, v142
	v_exp_f32_e32 v117, v143
	v_add_f32_e32 v114, v126, v144
	v_add_f32_e32 v115, v127, v145
	v_add_f32_e32 v140, v134, v152
	v_add_f32_e32 v141, v135, v153
	v_add_f32_e32 v142, v122, v154
	v_add_f32_e32 v143, v123, v155
	v_add_f32_e32 v212, v136, v120
	v_add_f32_e32 v213, v137, v121
	v_add_f32_e32 v214, v124, v116
	v_add_f32_e32 v215, v125, v117
	s_waitcnt lgkmcnt(4)
	v_mfma_f32_32x32x16_bf16 v[82:97], v[184:187], v[106:109], v[82:97]
	v_add_f32_e64 v184, v130, v148
	v_add_f32_e64 v185, v131, v149
	v_add_f32_e64 v186, v128, v146
	v_add_f32_e64 v187, v129, v147
	v_add_f32_e64 v216, v132, v150
	v_add_f32_e64 v217, v133, v151
	v_add_f32_e32 v186, v212, v186
	v_add_f32_e32 v187, v213, v187
	v_add_f32_e32 v214, v216, v214
	v_add_f32_e32 v215, v217, v215
	v_add_f32_e32 v142, v184, v142
	v_add_f32_e32 v143, v185, v143
	v_add_f32_e32 v114, v140, v114
	v_add_f32_e32 v115, v141, v115
	s_waitcnt lgkmcnt(3)
	v_mfma_f32_32x32x16_bf16 v[66:81], v[196:199], v[102:105], v[66:81]
	v_add_f32_e64 v114, v114, v142
	v_add_f32_e64 v115, v115, v143
	v_add_f32_e64 v140, v186, v214
	v_add_f32_e64 v141, v187, v215
	v_add_f32_e64 v114, v140, v114
	v_add_f32_e64 v115, v141, v115
	v_cvt_pk_bf16_f32 v140, v136, v137
	v_cvt_pk_bf16_f32 v141, v134, v135
	v_cvt_pk_bf16_f32 v142, v132, v133
	s_waitcnt lgkmcnt(2)
	v_mfma_f32_32x32x16_bf16 v[82:97], v[200:203], v[102:105], v[82:97]
	v_add_f32_e32 v240, v114, v115
	v_add_f32_e32 v115, v115, v114
	v_mov_b32_e32 v114, v240
	v_cvt_pk_bf16_f32 v143, v130, v131
	v_cvt_pk_bf16_f32 v128, v128, v129
	v_cvt_pk_bf16_f32 v129, v126, v127
	v_cvt_pk_bf16_f32 v130, v124, v125
	v_cvt_pk_bf16_f32 v131, v122, v123
	s_nop 0
	v_mov_b32_e32 v115, v114
	s_waitcnt lgkmcnt(1)
	v_mfma_f32_32x32x16_bf16 v[66:81], v[204:207], v[98:101], v[66:81]
	v_permlane32_swap_b32_e32 v114, v115
	v_cvt_pk_bf16_f32 v120, v120, v121
	v_cvt_pk_bf16_f32 v121, v152, v153
	v_cvt_pk_bf16_f32 v122, v150, v151
	v_cvt_pk_bf16_f32 v123, v148, v149
	v_cvt_pk_bf16_f32 v124, v146, v147
	s_waitcnt lgkmcnt(0)
	v_mfma_f32_32x32x16_bf16 v[82:97], v[208:211], v[98:101], v[82:97]
	v_cvt_pk_bf16_f32 v125, v144, v145
	v_cvt_pk_bf16_f32 v126, v116, v117
	v_cvt_pk_bf16_f32 v127, v154, v155
	v_permlane32_swap_b32_e32 v140, v142
	v_permlane32_swap_b32_e32 v141, v143
	v_permlane32_swap_b32_e32 v128, v130
	v_permlane32_swap_b32_e32 v129, v131
	v_permlane32_swap_b32_e32 v120, v122
	v_permlane32_swap_b32_e32 v121, v123
	v_permlane32_swap_b32_e32 v124, v126
	v_permlane32_swap_b32_e32 v125, v127
	ds_read_b64_tr_b16 v[132:133], v166 offset:0x8000
	ds_read_b64_tr_b16 v[134:135], v166 offset:0x8800
	ds_read_b64_tr_b16 v[144:145], v166 offset:0x9000
	ds_read_b64_tr_b16 v[146:147], v166 offset:0x9800
	ds_read_b64_tr_b16 v[148:149], v166 offset:0xa000
	ds_read_b64_tr_b16 v[150:151], v166 offset:0xa800
	ds_read_b64_tr_b16 v[152:153], v166 offset:0xb000
	ds_read_b64_tr_b16 v[154:155], v166 offset:0xb800
	ds_read_b64_tr_b16 v[184:185], v166 offset:0x8200
	ds_read_b64_tr_b16 v[186:187], v166 offset:0x8a00
	ds_read_b64_tr_b16 v[196:197], v166 offset:0x9200
	ds_read_b64_tr_b16 v[198:199], v166 offset:0x9a00
	ds_read_b64_tr_b16 v[200:201], v166 offset:0xa200
	ds_read_b64_tr_b16 v[202:203], v166 offset:0xaa00
	ds_read_b64_tr_b16 v[204:205], v166 offset:0xb200
	ds_read_b64_tr_b16 v[206:207], v166 offset:0xba00
	s_waitcnt lgkmcnt(8)
	s_nop 0
	v_mfma_f32_32x32x16_bf16 v[18:33], v[140:143], v[132:135], v[18:33]
	v_mfma_f32_32x32x16_bf16 v[18:33], v[128:131], v[144:147], v[18:33]
	v_mfma_f32_32x32x16_bf16 v[18:33], v[120:123], v[148:151], v[18:33]
	v_mfma_f32_32x32x16_bf16 v[18:33], v[124:127], v[152:155], v[18:33]
	ds_read_b64_tr_b16 v[132:133], v166 offset:0x8400
	ds_read_b64_tr_b16 v[134:135], v166 offset:0x8c00
	ds_read_b64_tr_b16 v[144:145], v166 offset:0x9400
	ds_read_b64_tr_b16 v[146:147], v166 offset:0x9c00
	ds_read_b64_tr_b16 v[148:149], v166 offset:0xa400
	ds_read_b64_tr_b16 v[150:151], v166 offset:0xac00
	ds_read_b64_tr_b16 v[152:153], v166 offset:0xb400
	ds_read_b64_tr_b16 v[154:155], v166 offset:0xbc00
	s_waitcnt lgkmcnt(8)
	v_mfma_f32_32x32x16_bf16 v[34:49], v[140:143], v[184:187], v[34:49]
	v_mfma_f32_32x32x16_bf16 v[34:49], v[128:131], v[196:199], v[34:49]
	v_mfma_f32_32x32x16_bf16 v[34:49], v[120:123], v[200:203], v[34:49]
	v_mfma_f32_32x32x16_bf16 v[34:49], v[124:127], v[204:207], v[34:49]
	ds_read_b64_tr_b16 v[184:185], v166 offset:0x8600
	ds_read_b64_tr_b16 v[186:187], v166 offset:0x8e00
	ds_read_b64_tr_b16 v[196:197], v166 offset:0x9600
	ds_read_b64_tr_b16 v[198:199], v166 offset:0x9e00
	ds_read_b64_tr_b16 v[200:201], v166 offset:0xa600
	ds_read_b64_tr_b16 v[202:203], v166 offset:0xae00
	ds_read_b64_tr_b16 v[204:205], v166 offset:0xb600
	ds_read_b64_tr_b16 v[206:207], v166 offset:0xbe00
	s_waitcnt lgkmcnt(8)
	v_mfma_f32_32x32x16_bf16 v[50:65], v[140:143], v[132:135], v[50:65]
	v_mfma_f32_32x32x16_bf16 v[50:65], v[128:131], v[144:147], v[50:65]
	v_mfma_f32_32x32x16_bf16 v[50:65], v[120:123], v[148:151], v[50:65]
	v_mfma_f32_32x32x16_bf16 v[50:65], v[124:127], v[152:155], v[50:65]
	s_waitcnt lgkmcnt(0)
	v_mfma_f32_32x32x16_bf16 v[2:17], v[140:143], v[184:187], v[2:17]
	s_add_i32 s6, s95, 0xffffff40
	s_cmp_le_i32 s6, s77
	v_mfma_f32_32x32x16_bf16 v[2:17], v[128:131], v[196:199], v[2:17]
	v_mfma_f32_32x32x16_bf16 v[2:17], v[120:123], v[200:203], v[2:17]
	v_mfma_f32_32x32x16_bf16 v[2:17], v[124:127], v[204:207], v[2:17]
	s_cbranch_scc1 .LBB0_253
	v_cmp_gt_i32_e64 s[66:67], 26, v183
	v_cmp_gt_i32_e64 s[68:69], 27, v183
	v_cmp_gt_i32_e64 s[64:65], 25, v183
	s_and_b64 s[66:67], s[68:69], s[66:67]
	v_cmp_gt_i32_e64 s[62:63], 24, v183
	s_and_b64 s[64:65], s[66:67], s[64:65]
	v_cmp_gt_i32_e64 s[60:61], 19, v183
	s_and_b64 s[62:63], s[64:65], s[62:63]
	v_cmp_gt_i32_e64 s[58:59], 18, v183
	s_and_b64 s[60:61], s[62:63], s[60:61]
	v_cmp_gt_i32_e64 s[56:57], 17, v183
	s_and_b64 s[58:59], s[60:61], s[58:59]
	v_cmp_gt_i32_e64 s[54:55], 16, v183
	s_and_b64 s[56:57], s[58:59], s[56:57]
	v_cmp_gt_i32_e64 s[52:53], 11, v183
	s_and_b64 s[54:55], s[56:57], s[54:55]
	v_cmp_gt_i32_e64 s[50:51], 10, v183
	s_and_b64 s[52:53], s[54:55], s[52:53]
	v_cmp_gt_i32_e64 s[48:49], 9, v183
	s_and_b64 s[50:51], s[52:53], s[50:51]
	v_cmp_gt_i32_e64 s[44:45], 8, v183
	s_and_b64 s[48:49], s[50:51], s[48:49]
	v_cmp_gt_i32_e64 s[42:43], 3, v183
	s_and_b64 s[44:45], s[48:49], s[44:45]
	v_cmp_gt_i32_e64 s[40:41], 2, v183
	s_and_b64 s[42:43], s[44:45], s[42:43]
	v_cmp_gt_i32_e64 s[38:39], 1, v183
	s_and_b64 s[40:41], s[42:43], s[40:41]
	v_cmp_gt_i32_e64 s[36:37], 0, v183
	s_and_b64 s[38:39], s[40:41], s[38:39]
	s_and_b64 s[36:37], s[38:39], s[36:37]
	v_cmp_gt_i32_e64 s[34:35], 58, v183
	v_cndmask_b32_e64 v66, v66, v160, s[36:37]
	v_cmp_gt_i32_e64 s[36:37], 59, v183
	v_cmp_gt_i32_e64 s[30:31], 57, v183
	s_and_b64 s[34:35], s[36:37], s[34:35]
	v_cmp_gt_i32_e64 s[28:29], 56, v183
	s_and_b64 s[30:31], s[34:35], s[30:31]
	v_cmp_gt_i32_e64 s[26:27], 51, v183
	s_and_b64 s[28:29], s[30:31], s[28:29]
	v_cmp_gt_i32_e64 s[24:25], 50, v183
	s_and_b64 s[26:27], s[28:29], s[26:27]
	v_cmp_gt_i32_e64 s[22:23], 49, v183
	s_and_b64 s[24:25], s[26:27], s[24:25]
	v_cmp_gt_i32_e64 s[20:21], 48, v183
	s_and_b64 s[22:23], s[24:25], s[22:23]
	v_cmp_gt_i32_e64 s[18:19], 43, v183
	s_and_b64 s[20:21], s[22:23], s[20:21]
	v_cmp_gt_i32_e64 s[16:17], 42, v183
	s_and_b64 s[18:19], s[20:21], s[18:19]
	v_cmp_gt_i32_e64 s[14:15], 41, v183
	s_and_b64 s[16:17], s[18:19], s[16:17]
	v_cmp_gt_i32_e64 s[12:13], 40, v183
	s_and_b64 s[14:15], s[16:17], s[14:15]
	v_cmp_gt_i32_e64 s[10:11], 35, v183
	s_and_b64 s[12:13], s[14:15], s[12:13]
	v_cmp_gt_i32_e64 s[8:9], 34, v183
	s_and_b64 s[10:11], s[12:13], s[10:11]
	v_cmp_gt_i32_e64 s[6:7], 33, v183
	s_and_b64 s[8:9], s[10:11], s[8:9]
	v_cmp_gt_i32_e32 vcc, 32, v183
	s_and_b64 s[6:7], s[8:9], s[6:7]
	s_and_b64 vcc, s[6:7], vcc
	v_cndmask_b32_e64 v81, v81, v160, s[68:69]
	v_cndmask_b32_e64 v80, v80, v160, s[66:67]
	v_cndmask_b32_e64 v79, v79, v160, s[64:65]
	v_cndmask_b32_e64 v78, v78, v160, s[62:63]
	v_cndmask_b32_e64 v77, v77, v160, s[60:61]
	v_cndmask_b32_e64 v76, v76, v160, s[58:59]
	v_cndmask_b32_e64 v75, v75, v160, s[56:57]
	v_cndmask_b32_e64 v74, v74, v160, s[54:55]
	v_cndmask_b32_e64 v73, v73, v160, s[52:53]
	v_cndmask_b32_e64 v72, v72, v160, s[50:51]
	v_cndmask_b32_e64 v71, v71, v160, s[48:49]
	v_cndmask_b32_e64 v70, v70, v160, s[44:45]
	v_cndmask_b32_e64 v69, v69, v160, s[42:43]
	v_cndmask_b32_e64 v68, v68, v160, s[40:41]
	v_cndmask_b32_e64 v67, v67, v160, s[38:39]
	v_cndmask_b32_e64 v97, v97, v160, s[36:37]
	v_cndmask_b32_e64 v96, v96, v160, s[34:35]
	v_cndmask_b32_e64 v95, v95, v160, s[30:31]
	v_cndmask_b32_e64 v94, v94, v160, s[28:29]
	v_cndmask_b32_e64 v93, v93, v160, s[26:27]
	v_cndmask_b32_e64 v92, v92, v160, s[24:25]
	v_cndmask_b32_e64 v91, v91, v160, s[22:23]
	v_cndmask_b32_e64 v90, v90, v160, s[20:21]
	v_cndmask_b32_e64 v89, v89, v160, s[18:19]
	v_cndmask_b32_e64 v88, v88, v160, s[16:17]
	v_cndmask_b32_e64 v87, v87, v160, s[14:15]
	v_cndmask_b32_e64 v86, v86, v160, s[12:13]
	v_cndmask_b32_e64 v85, v85, v160, s[10:11]
	v_cndmask_b32_e64 v84, v84, v160, s[8:9]
	v_cndmask_b32_e64 v83, v83, v160, s[6:7]
	v_cndmask_b32_e32 v82, v82, v160, vcc

.LBB0_257:
	v_cndmask_b32_e64 v120, v116, v139, s[6:7]
	s_waitcnt vmcnt(0)
	v_mul_f32_e32 v116, 0xbe38aa3b, v120
	v_fma_f32 v80, v80, s84, v116
	v_fma_f32 v81, v81, s84, v116
	v_fma_f32 v78, v78, s84, v116
	v_fma_f32 v79, v79, s84, v116
	v_fma_f32 v76, v76, s84, v116
	v_fma_f32 v77, v77, s84, v116
	v_fma_f32 v74, v74, s84, v116
	v_fma_f32 v75, v75, s84, v116
	v_fma_f32 v72, v72, s84, v116
	v_fma_f32 v73, v73, s84, v116
	v_fma_f32 v70, v70, s84, v116
	v_fma_f32 v71, v71, s84, v116
	v_fma_f32 v68, v68, s84, v116
	v_fma_f32 v69, v69, s84, v116
	v_fma_f32 v66, v66, s84, v116
	v_fma_f32 v67, v67, s84, v116
	v_fma_f32 v154, v88, s84, v116
	v_fma_f32 v155, v89, s84, v116
	v_fma_f32 v186, v86, s84, v116
	v_fma_f32 v187, v87, s84, v116
	v_fma_f32 v86, v84, s84, v116
	v_fma_f32 v87, v85, s84, v116
	v_fma_f32 v88, v82, s84, v116
	v_fma_f32 v89, v83, s84, v116
	v_fma_f32 v146, v96, s84, v116
	v_fma_f32 v147, v97, s84, v116
	v_fma_f32 v148, v94, s84, v116
	v_fma_f32 v149, v95, s84, v116
	v_fma_f32 v150, v92, s84, v116
	v_fma_f32 v151, v93, s84, v116
	v_fma_f32 v152, v90, s84, v116
	v_fma_f32 v153, v91, s84, v116
	v_exp_f32_e32 v196, v66
	v_exp_f32_e32 v197, v67
	v_exp_f32_e32 v198, v68
	v_exp_f32_e32 v199, v69
	v_exp_f32_e32 v200, v70
	v_exp_f32_e32 v201, v71
	v_exp_f32_e32 v202, v72
	v_exp_f32_e32 v203, v73
	v_exp_f32_e32 v204, v74
	v_exp_f32_e32 v205, v75
	v_exp_f32_e32 v206, v76
	v_exp_f32_e32 v207, v77
	v_exp_f32_e32 v208, v78
	v_exp_f32_e32 v209, v79
	v_exp_f32_e32 v210, v80
	v_exp_f32_e32 v211, v81
	s_barrier
	s_add_u32 s6, s72, 0x140000
	s_addc_u32 s7, s73, 0
	s_mov_b32 m0, s81
	s_nop 0
	global_load_lds_dwordx4 v168, s[6:7] offset:0
	s_add_u32 s6, s88, 0x140000
	s_addc_u32 s7, s89, 0
	s_mov_b32 m0, s74
	s_nop 0
	global_load_lds_dwordx4 v169, s[6:7] offset:0
	s_nop 0
	s_mov_b32 m0, s0
	s_nop 0
	global_load_lds_dwordx4 v170, s[6:7] offset:0
	ds_read_b128 v[66:69], v171
	ds_read_b128 v[82:85], v171 offset:4096
	ds_read_b128 v[122:125], v172
	ds_read_b128 v[126:129], v172 offset:4096
	v_exp_f32_e32 v212, v88
	s_waitcnt lgkmcnt(3)
	v_mfma_f32_32x32x16_bf16 v[66:81], v[66:69], v[110:113], 0
	v_exp_f32_e32 v213, v89
	v_exp_f32_e32 v214, v86
	v_exp_f32_e32 v215, v87
	ds_read_b128 v[130:133], v173
	ds_read_b128 v[134:137], v173 offset:4096
	ds_read_b128 v[138:141], v174
	ds_read_b128 v[142:145], v174 offset:4096
	v_exp_f32_e32 v186, v186
	v_exp_f32_e32 v187, v187
	v_exp_f32_e32 v154, v154
	s_waitcnt lgkmcnt(6)
	v_mfma_f32_32x32x16_bf16 v[82:97], v[82:85], v[110:113], 0
	v_exp_f32_e32 v155, v155
	v_exp_f32_e32 v152, v152
	v_exp_f32_e32 v153, v153
	v_exp_f32_e32 v150, v150
	v_exp_f32_e32 v151, v151
	v_exp_f32_e32 v148, v148
	v_exp_f32_e32 v149, v149
	s_waitcnt lgkmcnt(5)
	v_mfma_f32_32x32x16_bf16 v[66:81], v[122:125], v[106:109], v[66:81]
	v_exp_f32_e32 v146, v146
	v_exp_f32_e32 v147, v147
	v_add_f32_e32 v116, v206, v150
	v_add_f32_e32 v117, v207, v151
	v_add_f32_e32 v122, v198, v214
	v_add_f32_e32 v123, v199, v215
	v_add_f32_e32 v216, v196, v212
	v_add_f32_e32 v217, v197, v213
	v_add_f32_e32 v124, v210, v146
	v_add_f32_e32 v125, v211, v147
	v_add_f32_e32 v218, v208, v148
	v_add_f32_e32 v219, v209, v149
	s_waitcnt lgkmcnt(4)
	v_mfma_f32_32x32x16_bf16 v[82:97], v[126:129], v[106:109], v[82:97]
	v_add_f32_e64 v126, v202, v154
	v_add_f32_e64 v127, v203, v155
	v_add_f32_e64 v128, v204, v152
	v_add_f32_e64 v129, v205, v153
	v_add_f32_e64 v220, v200, v186
	v_add_f32_e64 v221, v201, v187
	v_add_f32_e32 v128, v216, v128
	v_add_f32_e32 v129, v217, v129
	v_add_f32_e32 v218, v220, v218
	v_add_f32_e32 v219, v221, v219
	v_add_f32_e32 v124, v126, v124
	v_add_f32_e32 v125, v127, v125
	v_add_f32_e32 v116, v122, v116
	v_add_f32_e32 v117, v123, v117
	s_waitcnt lgkmcnt(3)
	v_mfma_f32_32x32x16_bf16 v[66:81], v[130:133], v[102:105], v[66:81]
	v_add_f32_e64 v116, v116, v124
	v_add_f32_e64 v117, v117, v125
	v_add_f32_e64 v122, v128, v218
	v_add_f32_e64 v123, v129, v219
	v_add_f32_e64 v116, v122, v116
	v_add_f32_e64 v117, v123, v117
	v_cvt_pk_bf16_f32 v122, v196, v197
	v_cvt_pk_bf16_f32 v123, v198, v199
	v_cvt_pk_bf16_f32 v124, v200, v201
	s_waitcnt lgkmcnt(2)
	v_mfma_f32_32x32x16_bf16 v[82:97], v[134:137], v[102:105], v[82:97]
	v_add_f32_e32 v240, v116, v117
	v_add_f32_e32 v117, v117, v116
	v_mov_b32_e32 v116, v240
	v_cvt_pk_bf16_f32 v125, v202, v203
	v_cvt_pk_bf16_f32 v126, v204, v205
	v_cvt_pk_bf16_f32 v127, v206, v207
	v_cvt_pk_bf16_f32 v128, v208, v209
	v_cvt_pk_bf16_f32 v129, v210, v211
	s_nop 0
	v_mov_b32_e32 v117, v116
	s_waitcnt lgkmcnt(1)
	v_mfma_f32_32x32x16_bf16 v[66:81], v[138:141], v[98:101], v[66:81]
	v_permlane32_swap_b32_e32 v116, v117
	v_cvt_pk_bf16_f32 v130, v212, v213
	v_cvt_pk_bf16_f32 v131, v214, v215
	v_cvt_pk_bf16_f32 v132, v186, v187
	v_cvt_pk_bf16_f32 v133, v154, v155
	v_cvt_pk_bf16_f32 v134, v152, v153
	s_waitcnt lgkmcnt(0)
	v_mfma_f32_32x32x16_bf16 v[82:97], v[142:145], v[98:101], v[82:97]
	v_cvt_pk_bf16_f32 v135, v150, v151
	v_cvt_pk_bf16_f32 v136, v148, v149
	v_cvt_pk_bf16_f32 v137, v146, v147
	v_permlane32_swap_b32_e32 v122, v124
	v_permlane32_swap_b32_e32 v123, v125
	v_permlane32_swap_b32_e32 v126, v128
	v_permlane32_swap_b32_e32 v127, v129
	v_permlane32_swap_b32_e32 v130, v132
	v_permlane32_swap_b32_e32 v131, v133
	v_permlane32_swap_b32_e32 v134, v136
	v_permlane32_swap_b32_e32 v135, v137
	ds_read_b64_tr_b16 v[138:139], v166 offset:0xc000
	ds_read_b64_tr_b16 v[140:141], v166 offset:0xc800
	ds_read_b64_tr_b16 v[142:143], v166 offset:0xd000
	ds_read_b64_tr_b16 v[144:145], v166 offset:0xd800
	ds_read_b64_tr_b16 v[146:147], v166 offset:0xe000
	ds_read_b64_tr_b16 v[148:149], v166 offset:0xe800
	ds_read_b64_tr_b16 v[150:151], v166 offset:0xf000
	ds_read_b64_tr_b16 v[152:153], v166 offset:0xf800
	ds_read_b64_tr_b16 v[196:197], v166 offset:0xc200
	ds_read_b64_tr_b16 v[198:199], v166 offset:0xca00
	ds_read_b64_tr_b16 v[200:201], v166 offset:0xd200
	ds_read_b64_tr_b16 v[202:203], v166 offset:0xda00
	ds_read_b64_tr_b16 v[204:205], v166 offset:0xe200
	ds_read_b64_tr_b16 v[206:207], v166 offset:0xea00
	ds_read_b64_tr_b16 v[208:209], v166 offset:0xf200
	ds_read_b64_tr_b16 v[210:211], v166 offset:0xfa00
	s_waitcnt lgkmcnt(8)
	s_nop 0
	v_mfma_f32_32x32x16_bf16 v[18:33], v[122:125], v[138:141], v[18:33]
	v_mfma_f32_32x32x16_bf16 v[18:33], v[126:129], v[142:145], v[18:33]
	v_mfma_f32_32x32x16_bf16 v[18:33], v[130:133], v[146:149], v[18:33]
	v_mfma_f32_32x32x16_bf16 v[18:33], v[134:137], v[150:153], v[18:33]
	ds_read_b64_tr_b16 v[138:139], v166 offset:0xc400
	ds_read_b64_tr_b16 v[140:141], v166 offset:0xcc00
	ds_read_b64_tr_b16 v[142:143], v166 offset:0xd400
	ds_read_b64_tr_b16 v[144:145], v166 offset:0xdc00
	ds_read_b64_tr_b16 v[146:147], v166 offset:0xe400
	ds_read_b64_tr_b16 v[148:149], v166 offset:0xec00
	ds_read_b64_tr_b16 v[150:151], v166 offset:0xf400
	ds_read_b64_tr_b16 v[152:153], v166 offset:0xfc00
	s_waitcnt lgkmcnt(8)
	v_mfma_f32_32x32x16_bf16 v[34:49], v[122:125], v[196:199], v[34:49]
	v_mfma_f32_32x32x16_bf16 v[34:49], v[126:129], v[200:203], v[34:49]
	v_mfma_f32_32x32x16_bf16 v[34:49], v[130:133], v[204:207], v[34:49]
	v_mfma_f32_32x32x16_bf16 v[34:49], v[134:137], v[208:211], v[34:49]
	ds_read_b64_tr_b16 v[196:197], v166 offset:0xc600
	ds_read_b64_tr_b16 v[198:199], v166 offset:0xce00
	ds_read_b64_tr_b16 v[200:201], v166 offset:0xd600
	ds_read_b64_tr_b16 v[202:203], v166 offset:0xde00
	ds_read_b64_tr_b16 v[204:205], v166 offset:0xe600
	ds_read_b64_tr_b16 v[206:207], v166 offset:0xee00
	ds_read_b64_tr_b16 v[208:209], v166 offset:0xf600
	ds_read_b64_tr_b16 v[210:211], v166 offset:0xfe00
	s_waitcnt lgkmcnt(8)
	v_mfma_f32_32x32x16_bf16 v[50:65], v[122:125], v[138:141], v[50:65]
	v_mfma_f32_32x32x16_bf16 v[50:65], v[126:129], v[142:145], v[50:65]
	v_mfma_f32_32x32x16_bf16 v[50:65], v[130:133], v[146:149], v[50:65]
	v_mfma_f32_32x32x16_bf16 v[50:65], v[134:137], v[150:153], v[50:65]
	s_waitcnt lgkmcnt(0)
	v_mfma_f32_32x32x16_bf16 v[2:17], v[122:125], v[196:199], v[2:17]
	s_add_i32 s6, s95, 0xffffff80
	s_cmp_le_i32 s6, s77
	v_mfma_f32_32x32x16_bf16 v[2:17], v[126:129], v[200:203], v[2:17]
	v_mfma_f32_32x32x16_bf16 v[2:17], v[130:133], v[204:207], v[2:17]
	v_mfma_f32_32x32x16_bf16 v[2:17], v[134:137], v[208:211], v[2:17]
	s_cbranch_scc1 .LBB0_259
	v_subrev_u32_e32 v121, 64, v183
	v_cmp_gt_i32_e64 s[66:67], 26, v121
	v_cmp_gt_i32_e64 s[68:69], 27, v121
	v_cmp_gt_i32_e64 s[64:65], 25, v121
	s_and_b64 s[66:67], s[68:69], s[66:67]
	v_cmp_gt_i32_e64 s[62:63], 24, v121
	s_and_b64 s[64:65], s[66:67], s[64:65]
	v_cmp_gt_i32_e64 s[60:61], 19, v121
	s_and_b64 s[62:63], s[64:65], s[62:63]
	v_cmp_gt_i32_e64 s[58:59], 18, v121
	s_and_b64 s[60:61], s[62:63], s[60:61]
	v_cmp_gt_i32_e64 s[56:57], 17, v121
	s_and_b64 s[58:59], s[60:61], s[58:59]
	v_cmp_gt_i32_e64 s[54:55], 16, v121
	s_and_b64 s[56:57], s[58:59], s[56:57]
	v_cmp_gt_i32_e64 s[52:53], 11, v121
	s_and_b64 s[54:55], s[56:57], s[54:55]
	v_cmp_gt_i32_e64 s[50:51], 10, v121
	s_and_b64 s[52:53], s[54:55], s[52:53]
	v_cmp_gt_i32_e64 s[48:49], 9, v121
	s_and_b64 s[50:51], s[52:53], s[50:51]
	v_cmp_gt_i32_e64 s[44:45], 8, v121
	s_and_b64 s[48:49], s[50:51], s[48:49]
	v_cmp_gt_i32_e64 s[42:43], 3, v121
	s_and_b64 s[44:45], s[48:49], s[44:45]
	v_cmp_gt_i32_e64 s[40:41], 2, v121
	s_and_b64 s[42:43], s[44:45], s[42:43]
	v_cmp_gt_i32_e64 s[38:39], 1, v121
	s_and_b64 s[40:41], s[42:43], s[40:41]
	v_cmp_gt_i32_e64 s[36:37], 0, v121
	s_and_b64 s[38:39], s[40:41], s[38:39]
	s_and_b64 s[36:37], s[38:39], s[36:37]
	v_cmp_gt_i32_e64 s[34:35], 58, v121
	v_cndmask_b32_e64 v66, v66, v160, s[36:37]
	v_cmp_gt_i32_e64 s[36:37], 59, v121
	v_cmp_gt_i32_e64 s[30:31], 57, v121
	s_and_b64 s[34:35], s[36:37], s[34:35]
	v_cmp_gt_i32_e64 s[28:29], 56, v121
	s_and_b64 s[30:31], s[34:35], s[30:31]
	v_cmp_gt_i32_e64 s[26:27], 51, v121
	s_and_b64 s[28:29], s[30:31], s[28:29]
	v_cmp_gt_i32_e64 s[24:25], 50, v121
	s_and_b64 s[26:27], s[28:29], s[26:27]
	v_cmp_gt_i32_e64 s[22:23], 49, v121
	s_and_b64 s[24:25], s[26:27], s[24:25]
	v_cmp_gt_i32_e64 s[20:21], 48, v121
	s_and_b64 s[22:23], s[24:25], s[22:23]
	v_cmp_gt_i32_e64 s[18:19], 43, v121
	s_and_b64 s[20:21], s[22:23], s[20:21]
	v_cmp_gt_i32_e64 s[16:17], 42, v121
	s_and_b64 s[18:19], s[20:21], s[18:19]
	v_cmp_gt_i32_e64 s[14:15], 41, v121
	s_and_b64 s[16:17], s[18:19], s[16:17]
	v_cmp_gt_i32_e64 s[12:13], 40, v121
	s_and_b64 s[14:15], s[16:17], s[14:15]
	v_cmp_gt_i32_e64 s[10:11], 35, v121
	s_and_b64 s[12:13], s[14:15], s[12:13]
	v_cmp_gt_i32_e64 s[8:9], 34, v121
	s_and_b64 s[10:11], s[12:13], s[10:11]
	v_cmp_gt_i32_e64 s[6:7], 33, v121
	s_and_b64 s[8:9], s[10:11], s[8:9]
	v_cmp_gt_i32_e32 vcc, 32, v121
	s_and_b64 s[6:7], s[8:9], s[6:7]
	s_and_b64 vcc, s[6:7], vcc
	v_cndmask_b32_e64 v81, v81, v160, s[68:69]
	v_cndmask_b32_e64 v80, v80, v160, s[66:67]
	v_cndmask_b32_e64 v79, v79, v160, s[64:65]
	v_cndmask_b32_e64 v78, v78, v160, s[62:63]
	v_cndmask_b32_e64 v77, v77, v160, s[60:61]
	v_cndmask_b32_e64 v76, v76, v160, s[58:59]
	v_cndmask_b32_e64 v75, v75, v160, s[56:57]
	v_cndmask_b32_e64 v74, v74, v160, s[54:55]
	v_cndmask_b32_e64 v73, v73, v160, s[52:53]
	v_cndmask_b32_e64 v72, v72, v160, s[50:51]
	v_cndmask_b32_e64 v71, v71, v160, s[48:49]
	v_cndmask_b32_e64 v70, v70, v160, s[44:45]
	v_cndmask_b32_e64 v69, v69, v160, s[42:43]
	v_cndmask_b32_e64 v68, v68, v160, s[40:41]
	v_cndmask_b32_e64 v67, v67, v160, s[38:39]
	v_cndmask_b32_e64 v97, v97, v160, s[36:37]
	v_cndmask_b32_e64 v96, v96, v160, s[34:35]
	v_cndmask_b32_e64 v95, v95, v160, s[30:31]
	v_cndmask_b32_e64 v94, v94, v160, s[28:29]
	v_cndmask_b32_e64 v93, v93, v160, s[26:27]
	v_cndmask_b32_e64 v92, v92, v160, s[24:25]
	v_cndmask_b32_e64 v91, v91, v160, s[22:23]
	v_cndmask_b32_e64 v90, v90, v160, s[20:21]
	v_cndmask_b32_e64 v89, v89, v160, s[18:19]
	v_cndmask_b32_e64 v88, v88, v160, s[16:17]
	v_cndmask_b32_e64 v87, v87, v160, s[14:15]
	v_cndmask_b32_e64 v86, v86, v160, s[12:13]
	v_cndmask_b32_e64 v85, v85, v160, s[10:11]
	v_cndmask_b32_e64 v84, v84, v160, s[8:9]
	v_cndmask_b32_e64 v83, v83, v160, s[6:7]
	v_cndmask_b32_e32 v82, v82, v160, vcc

.LBB0_263:
	v_cndmask_b32_e64 v122, v121, v120, s[6:7]
	s_waitcnt vmcnt(0)
	v_mul_f32_e32 v120, 0xbe38aa3b, v122
	v_fma_f32 v80, v80, s84, v120
	v_fma_f32 v81, v81, s84, v120
	v_fma_f32 v78, v78, s84, v120
	v_fma_f32 v79, v79, s84, v120
	v_fma_f32 v76, v76, s84, v120
	v_fma_f32 v77, v77, s84, v120
	v_fma_f32 v74, v74, s84, v120
	v_fma_f32 v75, v75, s84, v120
	v_fma_f32 v72, v72, s84, v120
	v_fma_f32 v73, v73, s84, v120
	v_fma_f32 v70, v70, s84, v120
	v_fma_f32 v71, v71, s84, v120
	v_fma_f32 v68, v68, s84, v120
	v_fma_f32 v69, v69, s84, v120
	v_fma_f32 v66, v66, s84, v120
	v_fma_f32 v67, v67, s84, v120
	v_fma_f32 v186, v88, s84, v120
	v_fma_f32 v187, v89, s84, v120
	v_fma_f32 v196, v86, s84, v120
	v_fma_f32 v197, v87, s84, v120
	v_fma_f32 v86, v84, s84, v120
	v_fma_f32 v87, v85, s84, v120
	v_fma_f32 v88, v82, s84, v120
	v_fma_f32 v89, v83, s84, v120
	v_fma_f32 v148, v96, s84, v120
	v_fma_f32 v149, v97, s84, v120
	v_fma_f32 v150, v94, s84, v120
	v_fma_f32 v151, v95, s84, v120
	v_fma_f32 v152, v92, s84, v120
	v_fma_f32 v153, v93, s84, v120
	v_fma_f32 v154, v90, s84, v120
	v_fma_f32 v155, v91, s84, v120
	v_exp_f32_e32 v198, v66
	v_exp_f32_e32 v199, v67
	v_exp_f32_e32 v200, v68
	v_exp_f32_e32 v201, v69
	v_exp_f32_e32 v202, v70
	v_exp_f32_e32 v203, v71
	v_exp_f32_e32 v204, v72
	v_exp_f32_e32 v205, v73
	v_exp_f32_e32 v206, v74
	v_exp_f32_e32 v207, v75
	v_exp_f32_e32 v208, v76
	v_exp_f32_e32 v209, v77
	v_exp_f32_e32 v210, v78
	v_exp_f32_e32 v211, v79
	v_exp_f32_e32 v212, v80
	v_exp_f32_e32 v213, v81
	s_barrier
	s_add_u32 s6, s72, 0x180000
	s_addc_u32 s7, s73, 0
	s_mov_b32 m0, s85
	s_nop 0
	global_load_lds_dwordx4 v168, s[6:7] offset:0
	s_add_u32 s6, s88, 0x180000
	s_addc_u32 s7, s89, 0
	s_mov_b32 m0, s82
	s_nop 0
	global_load_lds_dwordx4 v169, s[6:7] offset:0
	s_nop 0
	s_mov_b32 m0, s83
	s_nop 0
	global_load_lds_dwordx4 v170, s[6:7] offset:0
	ds_read_b128 v[66:69], v175
	ds_read_b128 v[82:85], v175 offset:4096
	ds_read_b128 v[124:127], v176
	ds_read_b128 v[128:131], v176 offset:4096
	v_exp_f32_e32 v214, v88
	s_waitcnt lgkmcnt(3)
	v_mfma_f32_32x32x16_bf16 v[66:81], v[66:69], v[110:113], 0
	v_exp_f32_e32 v215, v89
	v_exp_f32_e32 v216, v86
	v_exp_f32_e32 v217, v87
	ds_read_b128 v[132:135], v177
	ds_read_b128 v[136:139], v177 offset:4096
	ds_read_b128 v[140:143], v178
	ds_read_b128 v[144:147], v178 offset:4096
	v_exp_f32_e32 v196, v196
	v_exp_f32_e32 v197, v197
	v_exp_f32_e32 v218, v186
	s_waitcnt lgkmcnt(6)
	v_mfma_f32_32x32x16_bf16 v[82:97], v[82:85], v[110:113], 0
	v_exp_f32_e32 v219, v187
	v_exp_f32_e32 v154, v154
	v_exp_f32_e32 v155, v155
	v_exp_f32_e32 v152, v152
	v_exp_f32_e32 v153, v153
	v_exp_f32_e32 v150, v150
	v_exp_f32_e32 v151, v151
	s_waitcnt lgkmcnt(5)
	v_mfma_f32_32x32x16_bf16 v[66:81], v[124:127], v[106:109], v[66:81]
	v_exp_f32_e32 v148, v148
	v_exp_f32_e32 v149, v149
	v_add_f32_e32 v120, v208, v152
	v_add_f32_e32 v121, v209, v153
	v_add_f32_e32 v124, v200, v216
	v_add_f32_e32 v125, v201, v217
	v_add_f32_e32 v186, v198, v214
	v_add_f32_e32 v187, v199, v215
	v_add_f32_e32 v126, v212, v148
	v_add_f32_e32 v127, v213, v149
	v_add_f32_e32 v220, v210, v150
	v_add_f32_e32 v221, v211, v151
	s_waitcnt lgkmcnt(4)
	v_mfma_f32_32x32x16_bf16 v[82:97], v[128:131], v[106:109], v[82:97]
	v_add_f32_e64 v128, v204, v218
	v_add_f32_e64 v129, v205, v219
	v_add_f32_e64 v130, v206, v154
	v_add_f32_e64 v131, v207, v155
	v_add_f32_e64 v222, v202, v196
	v_add_f32_e64 v223, v203, v197
	v_add_f32_e32 v130, v186, v130
	v_add_f32_e32 v131, v187, v131
	v_add_f32_e32 v220, v222, v220
	v_add_f32_e32 v221, v223, v221
	v_add_f32_e32 v126, v128, v126
	v_add_f32_e32 v127, v129, v127
	v_add_f32_e32 v120, v124, v120
	v_add_f32_e32 v121, v125, v121
	s_waitcnt lgkmcnt(3)
	v_mfma_f32_32x32x16_bf16 v[66:81], v[132:135], v[102:105], v[66:81]
	v_add_f32_e64 v120, v120, v126
	v_add_f32_e64 v121, v121, v127
	v_add_f32_e64 v124, v130, v220
	v_add_f32_e64 v125, v131, v221
	v_add_f32_e64 v120, v124, v120
	v_add_f32_e64 v121, v125, v121
	v_cvt_pk_bf16_f32 v124, v198, v199
	v_cvt_pk_bf16_f32 v125, v200, v201
	v_cvt_pk_bf16_f32 v126, v202, v203
	s_waitcnt lgkmcnt(2)
	v_mfma_f32_32x32x16_bf16 v[82:97], v[136:139], v[102:105], v[82:97]
	v_add_f32_e32 v240, v120, v121
	v_add_f32_e32 v121, v121, v120
	v_mov_b32_e32 v120, v240
	v_cvt_pk_bf16_f32 v127, v204, v205
	v_cvt_pk_bf16_f32 v128, v206, v207
	v_cvt_pk_bf16_f32 v129, v208, v209
	v_cvt_pk_bf16_f32 v130, v210, v211
	v_cvt_pk_bf16_f32 v131, v212, v213
	s_nop 0
	v_mov_b32_e32 v186, v120
	s_waitcnt lgkmcnt(1)
	v_mfma_f32_32x32x16_bf16 v[66:81], v[140:143], v[98:101], v[66:81]
	v_permlane32_swap_b32_e32 v120, v186
	v_cvt_pk_bf16_f32 v132, v214, v215
	v_cvt_pk_bf16_f32 v133, v216, v217
	v_cvt_pk_bf16_f32 v134, v196, v197
	v_cvt_pk_bf16_f32 v135, v218, v219
	v_cvt_pk_bf16_f32 v136, v154, v155
	s_waitcnt lgkmcnt(0)
	v_mfma_f32_32x32x16_bf16 v[82:97], v[144:147], v[98:101], v[82:97]
	v_cvt_pk_bf16_f32 v137, v152, v153
	v_cvt_pk_bf16_f32 v138, v150, v151
	v_cvt_pk_bf16_f32 v139, v148, v149
	v_permlane32_swap_b32_e32 v124, v126
	v_permlane32_swap_b32_e32 v125, v127
	v_permlane32_swap_b32_e32 v128, v130
	v_permlane32_swap_b32_e32 v129, v131
	v_permlane32_swap_b32_e32 v132, v134
	v_permlane32_swap_b32_e32 v133, v135
	v_permlane32_swap_b32_e32 v136, v138
	v_permlane32_swap_b32_e32 v137, v139
	ds_read_b64_tr_b16 v[140:141], v166 offset:0
	ds_read_b64_tr_b16 v[142:143], v166 offset:0x800
	ds_read_b64_tr_b16 v[144:145], v166 offset:0x1000
	ds_read_b64_tr_b16 v[146:147], v166 offset:0x1800
	ds_read_b64_tr_b16 v[148:149], v166 offset:0x2000
	ds_read_b64_tr_b16 v[150:151], v166 offset:0x2800
	ds_read_b64_tr_b16 v[152:153], v166 offset:0x3000
	ds_read_b64_tr_b16 v[154:155], v166 offset:0x3800
	ds_read_b64_tr_b16 v[196:197], v166 offset:0x200
	ds_read_b64_tr_b16 v[198:199], v166 offset:0xa00
	ds_read_b64_tr_b16 v[200:201], v166 offset:0x1200
	ds_read_b64_tr_b16 v[202:203], v166 offset:0x1a00
	ds_read_b64_tr_b16 v[204:205], v166 offset:0x2200
	ds_read_b64_tr_b16 v[206:207], v166 offset:0x2a00
	ds_read_b64_tr_b16 v[208:209], v166 offset:0x3200
	ds_read_b64_tr_b16 v[210:211], v166 offset:0x3a00
	s_waitcnt lgkmcnt(8)
	s_nop 0
	v_mfma_f32_32x32x16_bf16 v[18:33], v[124:127], v[140:143], v[18:33]
	v_mfma_f32_32x32x16_bf16 v[18:33], v[128:131], v[144:147], v[18:33]
	v_mfma_f32_32x32x16_bf16 v[18:33], v[132:135], v[148:151], v[18:33]
	v_mfma_f32_32x32x16_bf16 v[18:33], v[136:139], v[152:155], v[18:33]
	ds_read_b64_tr_b16 v[140:141], v166 offset:0x400
	ds_read_b64_tr_b16 v[142:143], v166 offset:0xc00
	ds_read_b64_tr_b16 v[144:145], v166 offset:0x1400
	ds_read_b64_tr_b16 v[146:147], v166 offset:0x1c00
	ds_read_b64_tr_b16 v[148:149], v166 offset:0x2400
	ds_read_b64_tr_b16 v[150:151], v166 offset:0x2c00
	ds_read_b64_tr_b16 v[152:153], v166 offset:0x3400
	ds_read_b64_tr_b16 v[154:155], v166 offset:0x3c00
	s_waitcnt lgkmcnt(8)
	v_mfma_f32_32x32x16_bf16 v[34:49], v[124:127], v[196:199], v[34:49]
	v_mfma_f32_32x32x16_bf16 v[34:49], v[128:131], v[200:203], v[34:49]
	v_mfma_f32_32x32x16_bf16 v[34:49], v[132:135], v[204:207], v[34:49]
	v_mfma_f32_32x32x16_bf16 v[34:49], v[136:139], v[208:211], v[34:49]
	ds_read_b64_tr_b16 v[196:197], v166 offset:0x600
	ds_read_b64_tr_b16 v[198:199], v166 offset:0xe00
	ds_read_b64_tr_b16 v[200:201], v166 offset:0x1600
	ds_read_b64_tr_b16 v[202:203], v166 offset:0x1e00
	ds_read_b64_tr_b16 v[204:205], v166 offset:0x2600
	ds_read_b64_tr_b16 v[206:207], v166 offset:0x2e00
	ds_read_b64_tr_b16 v[208:209], v166 offset:0x3600
	ds_read_b64_tr_b16 v[210:211], v166 offset:0x3e00
	s_waitcnt lgkmcnt(8)
	v_mfma_f32_32x32x16_bf16 v[50:65], v[124:127], v[140:143], v[50:65]
	v_mfma_f32_32x32x16_bf16 v[50:65], v[128:131], v[144:147], v[50:65]
	v_mfma_f32_32x32x16_bf16 v[50:65], v[132:135], v[148:151], v[50:65]
	v_mfma_f32_32x32x16_bf16 v[50:65], v[136:139], v[152:155], v[50:65]
	s_waitcnt lgkmcnt(0)
	v_mfma_f32_32x32x16_bf16 v[2:17], v[124:127], v[196:199], v[2:17]
	s_sub_i32 s6, s95, 64
	s_cmp_le_i32 s6, s77
	v_mfma_f32_32x32x16_bf16 v[2:17], v[128:131], v[200:203], v[2:17]
	v_mfma_f32_32x32x16_bf16 v[2:17], v[132:135], v[204:207], v[2:17]
	v_mfma_f32_32x32x16_bf16 v[2:17], v[136:139], v[208:211], v[2:17]
	s_cbranch_scc1 .LBB0_265
	v_add_u32_e32 v121, 0xffffff80, v183
	v_cmp_gt_i32_e64 s[66:67], 26, v121
	v_cmp_gt_i32_e64 s[68:69], 27, v121
	v_cmp_gt_i32_e64 s[64:65], 25, v121
	s_and_b64 s[66:67], s[68:69], s[66:67]
	v_cmp_gt_i32_e64 s[62:63], 24, v121
	s_and_b64 s[64:65], s[66:67], s[64:65]
	v_cmp_gt_i32_e64 s[60:61], 19, v121
	s_and_b64 s[62:63], s[64:65], s[62:63]
	v_cmp_gt_i32_e64 s[58:59], 18, v121
	s_and_b64 s[60:61], s[62:63], s[60:61]
	v_cmp_gt_i32_e64 s[56:57], 17, v121
	s_and_b64 s[58:59], s[60:61], s[58:59]
	v_cmp_gt_i32_e64 s[54:55], 16, v121
	s_and_b64 s[56:57], s[58:59], s[56:57]
	v_cmp_gt_i32_e64 s[52:53], 11, v121
	s_and_b64 s[54:55], s[56:57], s[54:55]
	v_cmp_gt_i32_e64 s[50:51], 10, v121
	s_and_b64 s[52:53], s[54:55], s[52:53]
	v_cmp_gt_i32_e64 s[48:49], 9, v121
	s_and_b64 s[50:51], s[52:53], s[50:51]
	v_cmp_gt_i32_e64 s[44:45], 8, v121
	s_and_b64 s[48:49], s[50:51], s[48:49]
	v_cmp_gt_i32_e64 s[42:43], 3, v121
	s_and_b64 s[44:45], s[48:49], s[44:45]
	v_cmp_gt_i32_e64 s[40:41], 2, v121
	s_and_b64 s[42:43], s[44:45], s[42:43]
	v_cmp_gt_i32_e64 s[38:39], 1, v121
	s_and_b64 s[40:41], s[42:43], s[40:41]
	v_cmp_gt_i32_e64 s[36:37], 0, v121
	s_and_b64 s[38:39], s[40:41], s[38:39]
	s_and_b64 s[36:37], s[38:39], s[36:37]
	v_cmp_gt_i32_e64 s[34:35], 58, v121
	v_cndmask_b32_e64 v66, v66, v160, s[36:37]
	v_cmp_gt_i32_e64 s[36:37], 59, v121
	v_cmp_gt_i32_e64 s[30:31], 57, v121
	s_and_b64 s[34:35], s[36:37], s[34:35]
	v_cmp_gt_i32_e64 s[28:29], 56, v121
	s_and_b64 s[30:31], s[34:35], s[30:31]
	v_cmp_gt_i32_e64 s[26:27], 51, v121
	s_and_b64 s[28:29], s[30:31], s[28:29]
	v_cmp_gt_i32_e64 s[24:25], 50, v121
	s_and_b64 s[26:27], s[28:29], s[26:27]
	v_cmp_gt_i32_e64 s[22:23], 49, v121
	s_and_b64 s[24:25], s[26:27], s[24:25]
	v_cmp_gt_i32_e64 s[20:21], 48, v121
	s_and_b64 s[22:23], s[24:25], s[22:23]
	v_cmp_gt_i32_e64 s[18:19], 43, v121
	s_and_b64 s[20:21], s[22:23], s[20:21]
	v_cmp_gt_i32_e64 s[16:17], 42, v121
	s_and_b64 s[18:19], s[20:21], s[18:19]
	v_cmp_gt_i32_e64 s[14:15], 41, v121
	s_and_b64 s[16:17], s[18:19], s[16:17]
	v_cmp_gt_i32_e64 s[12:13], 40, v121
	s_and_b64 s[14:15], s[16:17], s[14:15]
	v_cmp_gt_i32_e64 s[10:11], 35, v121
	s_and_b64 s[12:13], s[14:15], s[12:13]
	v_cmp_gt_i32_e64 s[8:9], 34, v121
	s_and_b64 s[10:11], s[12:13], s[10:11]
	v_cmp_gt_i32_e64 s[6:7], 33, v121
	s_and_b64 s[8:9], s[10:11], s[8:9]
	v_cmp_gt_i32_e32 vcc, 32, v121
	s_and_b64 s[6:7], s[8:9], s[6:7]
	s_and_b64 vcc, s[6:7], vcc
	v_cndmask_b32_e64 v81, v81, v160, s[68:69]
	v_cndmask_b32_e64 v80, v80, v160, s[66:67]
	v_cndmask_b32_e64 v79, v79, v160, s[64:65]
	v_cndmask_b32_e64 v78, v78, v160, s[62:63]
	v_cndmask_b32_e64 v77, v77, v160, s[60:61]
	v_cndmask_b32_e64 v76, v76, v160, s[58:59]
	v_cndmask_b32_e64 v75, v75, v160, s[56:57]
	v_cndmask_b32_e64 v74, v74, v160, s[54:55]
	v_cndmask_b32_e64 v73, v73, v160, s[52:53]
	v_cndmask_b32_e64 v72, v72, v160, s[50:51]
	v_cndmask_b32_e64 v71, v71, v160, s[48:49]
	v_cndmask_b32_e64 v70, v70, v160, s[44:45]
	v_cndmask_b32_e64 v69, v69, v160, s[42:43]
	v_cndmask_b32_e64 v68, v68, v160, s[40:41]
	v_cndmask_b32_e64 v67, v67, v160, s[38:39]
	v_cndmask_b32_e64 v97, v97, v160, s[36:37]
	v_cndmask_b32_e64 v96, v96, v160, s[34:35]
	v_cndmask_b32_e64 v95, v95, v160, s[30:31]
	v_cndmask_b32_e64 v94, v94, v160, s[28:29]
	v_cndmask_b32_e64 v93, v93, v160, s[26:27]
	v_cndmask_b32_e64 v92, v92, v160, s[24:25]
	v_cndmask_b32_e64 v91, v91, v160, s[22:23]
	v_cndmask_b32_e64 v90, v90, v160, s[20:21]
	v_cndmask_b32_e64 v89, v89, v160, s[18:19]
	v_cndmask_b32_e64 v88, v88, v160, s[16:17]
	v_cndmask_b32_e64 v87, v87, v160, s[14:15]
	v_cndmask_b32_e64 v86, v86, v160, s[12:13]
	v_cndmask_b32_e64 v85, v85, v160, s[10:11]
	v_cndmask_b32_e64 v84, v84, v160, s[8:9]
	v_cndmask_b32_e64 v83, v83, v160, s[6:7]
	v_cndmask_b32_e32 v82, v82, v160, vcc

.LBB0_269:
	v_cndmask_b32_e64 v121, v121, v122, s[6:7]
	s_waitcnt vmcnt(0)
	v_mul_f32_e32 v122, 0xbe38aa3b, v121
	v_fma_f32 v80, v80, s84, v122
	v_fma_f32 v81, v81, s84, v122
	v_fma_f32 v78, v78, s84, v122
	v_fma_f32 v79, v79, s84, v122
	v_fma_f32 v76, v76, s84, v122
	v_fma_f32 v77, v77, s84, v122
	v_fma_f32 v74, v74, s84, v122
	v_fma_f32 v75, v75, s84, v122
	v_fma_f32 v72, v72, s84, v122
	v_fma_f32 v73, v73, s84, v122
	v_fma_f32 v70, v70, s84, v122
	v_fma_f32 v71, v71, s84, v122
	v_fma_f32 v68, v68, s84, v122
	v_fma_f32 v69, v69, s84, v122
	v_fma_f32 v66, v66, s84, v122
	v_fma_f32 v67, v67, s84, v122
	v_fma_f32 v138, v96, s84, v122
	v_fma_f32 v139, v97, s84, v122
	v_fma_f32 v148, v94, s84, v122
	v_fma_f32 v149, v95, s84, v122
	v_fma_f32 v150, v92, s84, v122
	v_fma_f32 v151, v93, s84, v122
	v_fma_f32 v152, v90, s84, v122
	v_fma_f32 v153, v91, s84, v122
	v_fma_f32 v154, v88, s84, v122
	v_fma_f32 v155, v89, s84, v122
	v_fma_f32 v196, v86, s84, v122
	v_fma_f32 v197, v87, s84, v122
	v_fma_f32 v198, v84, s84, v122
	v_fma_f32 v199, v85, s84, v122
	v_fma_f32 v200, v82, s84, v122
	v_fma_f32 v201, v83, s84, v122
	v_exp_f32_e32 v202, v66
	v_exp_f32_e32 v203, v67
	v_exp_f32_e32 v204, v68
	v_exp_f32_e32 v205, v69
	v_exp_f32_e32 v206, v70
	v_exp_f32_e32 v207, v71
	v_exp_f32_e32 v208, v72
	v_exp_f32_e32 v209, v73
	v_exp_f32_e32 v210, v74
	v_exp_f32_e32 v211, v75
	v_exp_f32_e32 v212, v76
	v_exp_f32_e32 v213, v77
	v_exp_f32_e32 v214, v78
	v_exp_f32_e32 v215, v79
	v_exp_f32_e32 v216, v80
	v_exp_f32_e32 v217, v81
	s_barrier
	s_add_u32 s6, s72, 0x1c0000
	s_addc_u32 s7, s73, 0
	s_mov_b32 m0, s81
	s_nop 0
	global_load_lds_dwordx4 v168, s[6:7] offset:0
	s_add_u32 s6, s88, 0x1c0000
	s_addc_u32 s7, s89, 0
	s_mov_b32 m0, s78
	s_nop 0
	global_load_lds_dwordx4 v169, s[6:7] offset:0
	s_nop 0
	s_mov_b32 m0, s79
	s_nop 0
	global_load_lds_dwordx4 v170, s[6:7] offset:0
	ds_read_b128 v[66:69], v171
	ds_read_b128 v[70:73], v171 offset:4096
	ds_read_b128 v[122:125], v172
	ds_read_b128 v[126:129], v172 offset:4096
	ds_read_b128 v[130:133], v173
	ds_read_b128 v[134:137], v173 offset:4096
	ds_read_b128 v[140:143], v174
	ds_read_b128 v[144:147], v174 offset:4096
	s_waitcnt lgkmcnt(7)
	v_mfma_f32_32x32x16_bf16 v[82:97], v[66:69], v[110:113], 0
	v_exp_f32_e32 v200, v200
	v_exp_f32_e32 v201, v201
	v_exp_f32_e32 v198, v198
	v_exp_f32_e32 v199, v199
	v_exp_f32_e32 v196, v196
	v_exp_f32_e32 v197, v197
	v_exp_f32_e32 v154, v154
	s_waitcnt lgkmcnt(6)
	v_mfma_f32_32x32x16_bf16 v[66:81], v[70:73], v[110:113], 0
	v_exp_f32_e32 v155, v155
	v_exp_f32_e32 v152, v152
	v_exp_f32_e32 v153, v153
	v_exp_f32_e32 v150, v150
	v_exp_f32_e32 v151, v151
	v_exp_f32_e32 v148, v148
	v_exp_f32_e32 v149, v149
	s_waitcnt lgkmcnt(5)
	v_mfma_f32_32x32x16_bf16 v[82:97], v[122:125], v[106:109], v[82:97]
	v_exp_f32_e32 v218, v138
	v_exp_f32_e32 v219, v139
	v_add_f32_e32 v122, v212, v150
	v_add_f32_e32 v123, v213, v151
	v_add_f32_e32 v124, v204, v198
	v_add_f32_e32 v125, v205, v199
	v_add_f32_e32 v138, v210, v152
	v_add_f32_e32 v139, v211, v153
	v_add_f32_e32 v220, v202, v200
	v_add_f32_e32 v221, v203, v201
	v_add_f32_e32 v222, v214, v148
	v_add_f32_e32 v223, v215, v149
	s_waitcnt lgkmcnt(4)
	v_mfma_f32_32x32x16_bf16 v[66:81], v[126:129], v[106:109], v[66:81]
	v_add_f32_e64 v126, v216, v218
	v_add_f32_e64 v127, v217, v219
	v_add_f32_e64 v128, v208, v154
	v_add_f32_e64 v129, v209, v155
	v_add_f32_e64 v224, v206, v196
	v_add_f32_e64 v225, v207, v197
	v_add_f32_e32 v126, v128, v126
	v_add_f32_e32 v127, v129, v127
	v_add_f32_e32 v222, v224, v222
	v_add_f32_e32 v223, v225, v223
	v_add_f32_e32 v122, v124, v122
	v_add_f32_e32 v123, v125, v123
	s_waitcnt lgkmcnt(3)
	v_mfma_f32_32x32x16_bf16 v[82:97], v[130:133], v[102:105], v[82:97]
	v_add_f32_e64 v130, v220, v138
	v_add_f32_e64 v131, v221, v139
	v_add_f32_e64 v122, v122, v126
	v_add_f32_e64 v123, v123, v127
	v_add_f32_e64 v124, v130, v222
	v_add_f32_e64 v125, v131, v223
	v_add_f32_e32 v122, v124, v122
	v_add_f32_e32 v123, v125, v123
	s_nop 0
	v_add_f32_e32 v138, v122, v123
	v_add_f32_e32 v139, v123, v122
	s_waitcnt lgkmcnt(2)
	v_mfma_f32_32x32x16_bf16 v[66:81], v[134:137], v[102:105], v[66:81]
	v_mov_b32_e32 v195, v138
	s_nop 1
	v_permlane32_swap_b32_e32 v138, v195
	v_cvt_pk_bf16_f32 v122, v202, v203
	v_cvt_pk_bf16_f32 v123, v204, v205
	v_cvt_pk_bf16_f32 v124, v206, v207
	v_cvt_pk_bf16_f32 v125, v208, v209
	s_waitcnt lgkmcnt(1)
	v_mfma_f32_32x32x16_bf16 v[82:97], v[140:143], v[98:101], v[82:97]
	v_cvt_pk_bf16_f32 v126, v210, v211
	v_cvt_pk_bf16_f32 v127, v212, v213
	v_cvt_pk_bf16_f32 v128, v214, v215
	v_cvt_pk_bf16_f32 v129, v216, v217
	v_cvt_pk_bf16_f32 v130, v200, v201
	v_cvt_pk_bf16_f32 v131, v198, v199
	v_cvt_pk_bf16_f32 v132, v196, v197
	s_waitcnt lgkmcnt(0)
	v_mfma_f32_32x32x16_bf16 v[66:81], v[144:147], v[98:101], v[66:81]
	v_cvt_pk_bf16_f32 v133, v154, v155
	v_cvt_pk_bf16_f32 v134, v152, v153
	v_cvt_pk_bf16_f32 v135, v150, v151
	v_cvt_pk_bf16_f32 v136, v148, v149
	v_cvt_pk_bf16_f32 v137, v218, v219
	v_permlane32_swap_b32_e32 v122, v124
	v_permlane32_swap_b32_e32 v123, v125
	v_permlane32_swap_b32_e32 v126, v128
	v_permlane32_swap_b32_e32 v127, v129
	v_permlane32_swap_b32_e32 v130, v132
	v_permlane32_swap_b32_e32 v131, v133
	v_permlane32_swap_b32_e32 v134, v136
	v_permlane32_swap_b32_e32 v135, v137
	ds_read_b64_tr_b16 v[140:141], v166 offset:0x4000
	ds_read_b64_tr_b16 v[142:143], v166 offset:0x4800
	ds_read_b64_tr_b16 v[144:145], v166 offset:0x5000
	ds_read_b64_tr_b16 v[146:147], v166 offset:0x5800
	ds_read_b64_tr_b16 v[148:149], v166 offset:0x6000
	ds_read_b64_tr_b16 v[150:151], v166 offset:0x6800
	ds_read_b64_tr_b16 v[152:153], v166 offset:0x7000
	ds_read_b64_tr_b16 v[154:155], v166 offset:0x7800
	ds_read_b64_tr_b16 v[196:197], v166 offset:0x4200
	ds_read_b64_tr_b16 v[198:199], v166 offset:0x4a00
	ds_read_b64_tr_b16 v[200:201], v166 offset:0x5200
	ds_read_b64_tr_b16 v[202:203], v166 offset:0x5a00
	ds_read_b64_tr_b16 v[204:205], v166 offset:0x6200
	ds_read_b64_tr_b16 v[206:207], v166 offset:0x6a00
	ds_read_b64_tr_b16 v[208:209], v166 offset:0x7200
	ds_read_b64_tr_b16 v[210:211], v166 offset:0x7a00
	s_waitcnt lgkmcnt(8)
	s_nop 0
	v_mfma_f32_32x32x16_bf16 v[18:33], v[122:125], v[140:143], v[18:33]
	v_mfma_f32_32x32x16_bf16 v[18:33], v[126:129], v[144:147], v[18:33]
	v_mfma_f32_32x32x16_bf16 v[18:33], v[130:133], v[148:151], v[18:33]
	v_mfma_f32_32x32x16_bf16 v[18:33], v[134:137], v[152:155], v[18:33]
	ds_read_b64_tr_b16 v[140:141], v166 offset:0x4400
	ds_read_b64_tr_b16 v[142:143], v166 offset:0x4c00
	ds_read_b64_tr_b16 v[144:145], v166 offset:0x5400
	ds_read_b64_tr_b16 v[146:147], v166 offset:0x5c00
	ds_read_b64_tr_b16 v[148:149], v166 offset:0x6400
	ds_read_b64_tr_b16 v[150:151], v166 offset:0x6c00
	ds_read_b64_tr_b16 v[152:153], v166 offset:0x7400
	ds_read_b64_tr_b16 v[154:155], v166 offset:0x7c00
	s_waitcnt lgkmcnt(8)
	v_mfma_f32_32x32x16_bf16 v[34:49], v[122:125], v[196:199], v[34:49]
	v_mfma_f32_32x32x16_bf16 v[34:49], v[126:129], v[200:203], v[34:49]
	v_mfma_f32_32x32x16_bf16 v[34:49], v[130:133], v[204:207], v[34:49]
	v_mfma_f32_32x32x16_bf16 v[34:49], v[134:137], v[208:211], v[34:49]
	ds_read_b64_tr_b16 v[196:197], v166 offset:0x4600
	ds_read_b64_tr_b16 v[198:199], v166 offset:0x4e00
	ds_read_b64_tr_b16 v[200:201], v166 offset:0x5600
	ds_read_b64_tr_b16 v[202:203], v166 offset:0x5e00
	ds_read_b64_tr_b16 v[204:205], v166 offset:0x6600
	ds_read_b64_tr_b16 v[206:207], v166 offset:0x6e00
	ds_read_b64_tr_b16 v[208:209], v166 offset:0x7600
	ds_read_b64_tr_b16 v[210:211], v166 offset:0x7e00
	s_waitcnt lgkmcnt(8)
	v_mfma_f32_32x32x16_bf16 v[50:65], v[122:125], v[140:143], v[50:65]
	v_mfma_f32_32x32x16_bf16 v[50:65], v[126:129], v[144:147], v[50:65]
	v_mfma_f32_32x32x16_bf16 v[50:65], v[130:133], v[148:151], v[50:65]
	v_mfma_f32_32x32x16_bf16 v[50:65], v[134:137], v[152:155], v[50:65]
	s_waitcnt lgkmcnt(0)
	v_mfma_f32_32x32x16_bf16 v[2:17], v[122:125], v[196:199], v[2:17]
	s_cmp_le_i32 s95, s77
	v_mfma_f32_32x32x16_bf16 v[2:17], v[126:129], v[200:203], v[2:17]
	v_mfma_f32_32x32x16_bf16 v[2:17], v[130:133], v[204:207], v[2:17]
	v_mfma_f32_32x32x16_bf16 v[2:17], v[134:137], v[208:211], v[2:17]
	s_cbranch_scc1 .LBB0_271
	v_add_u32_e32 v122, 0xffffff40, v183
	v_cmp_gt_i32_e64 s[66:67], 26, v122
	v_cmp_gt_i32_e64 s[68:69], 27, v122
	v_cmp_gt_i32_e64 s[64:65], 25, v122
	s_and_b64 s[66:67], s[68:69], s[66:67]
	v_cmp_gt_i32_e64 s[62:63], 24, v122
	s_and_b64 s[64:65], s[66:67], s[64:65]
	v_cmp_gt_i32_e64 s[60:61], 19, v122
	s_and_b64 s[62:63], s[64:65], s[62:63]
	v_cmp_gt_i32_e64 s[58:59], 18, v122
	s_and_b64 s[60:61], s[62:63], s[60:61]
	v_cmp_gt_i32_e64 s[56:57], 17, v122
	s_and_b64 s[58:59], s[60:61], s[58:59]
	v_cmp_gt_i32_e64 s[54:55], 16, v122
	s_and_b64 s[56:57], s[58:59], s[56:57]
	v_cmp_gt_i32_e64 s[52:53], 11, v122
	s_and_b64 s[54:55], s[56:57], s[54:55]
	v_cmp_gt_i32_e64 s[50:51], 10, v122
	s_and_b64 s[52:53], s[54:55], s[52:53]
	v_cmp_gt_i32_e64 s[48:49], 9, v122
	s_and_b64 s[50:51], s[52:53], s[50:51]
	v_cmp_gt_i32_e64 s[44:45], 8, v122
	s_and_b64 s[48:49], s[50:51], s[48:49]
	v_cmp_gt_i32_e64 s[42:43], 3, v122
	s_and_b64 s[44:45], s[48:49], s[44:45]
	v_cmp_gt_i32_e64 s[40:41], 2, v122
	s_and_b64 s[42:43], s[44:45], s[42:43]
	v_cmp_gt_i32_e64 s[38:39], 1, v122
	s_and_b64 s[40:41], s[42:43], s[40:41]
	v_cmp_gt_i32_e64 s[36:37], 0, v122
	s_and_b64 s[38:39], s[40:41], s[38:39]
	s_and_b64 s[36:37], s[38:39], s[36:37]
	v_cmp_gt_i32_e64 s[34:35], 58, v122
	v_cndmask_b32_e64 v82, v82, v160, s[36:37]
	v_cmp_gt_i32_e64 s[36:37], 59, v122
	v_cmp_gt_i32_e64 s[30:31], 57, v122
	s_and_b64 s[34:35], s[36:37], s[34:35]
	v_cmp_gt_i32_e64 s[28:29], 56, v122
	s_and_b64 s[30:31], s[34:35], s[30:31]
	v_cmp_gt_i32_e64 s[26:27], 51, v122
	s_and_b64 s[28:29], s[30:31], s[28:29]
	v_cmp_gt_i32_e64 s[24:25], 50, v122
	s_and_b64 s[26:27], s[28:29], s[26:27]
	v_cmp_gt_i32_e64 s[22:23], 49, v122
	s_and_b64 s[24:25], s[26:27], s[24:25]
	v_cmp_gt_i32_e64 s[20:21], 48, v122
	s_and_b64 s[22:23], s[24:25], s[22:23]
	v_cmp_gt_i32_e64 s[18:19], 43, v122
	s_and_b64 s[20:21], s[22:23], s[20:21]
	v_cmp_gt_i32_e64 s[16:17], 42, v122
	s_and_b64 s[18:19], s[20:21], s[18:19]
	v_cmp_gt_i32_e64 s[14:15], 41, v122
	s_and_b64 s[16:17], s[18:19], s[16:17]
	v_cmp_gt_i32_e64 s[12:13], 40, v122
	s_and_b64 s[14:15], s[16:17], s[14:15]
	v_cmp_gt_i32_e64 s[10:11], 35, v122
	s_and_b64 s[12:13], s[14:15], s[12:13]
	v_cmp_gt_i32_e64 s[8:9], 34, v122
	s_and_b64 s[10:11], s[12:13], s[10:11]
	v_cmp_gt_i32_e64 s[6:7], 33, v122
	s_and_b64 s[8:9], s[10:11], s[8:9]
	v_cmp_gt_i32_e32 vcc, 32, v122
	s_and_b64 s[6:7], s[8:9], s[6:7]
	s_and_b64 vcc, s[6:7], vcc
	v_cndmask_b32_e64 v97, v97, v160, s[68:69]
	v_cndmask_b32_e64 v96, v96, v160, s[66:67]
	v_cndmask_b32_e64 v95, v95, v160, s[64:65]
	v_cndmask_b32_e64 v94, v94, v160, s[62:63]
	v_cndmask_b32_e64 v93, v93, v160, s[60:61]
	v_cndmask_b32_e64 v92, v92, v160, s[58:59]
	v_cndmask_b32_e64 v91, v91, v160, s[56:57]
	v_cndmask_b32_e64 v90, v90, v160, s[54:55]
	v_cndmask_b32_e64 v89, v89, v160, s[52:53]
	v_cndmask_b32_e64 v88, v88, v160, s[50:51]
	v_cndmask_b32_e64 v87, v87, v160, s[48:49]
	v_cndmask_b32_e64 v86, v86, v160, s[44:45]
	v_cndmask_b32_e64 v85, v85, v160, s[42:43]
	v_cndmask_b32_e64 v84, v84, v160, s[40:41]
	v_cndmask_b32_e64 v83, v83, v160, s[38:39]
	v_cndmask_b32_e64 v81, v81, v160, s[36:37]
	v_cndmask_b32_e64 v80, v80, v160, s[34:35]
	v_cndmask_b32_e64 v79, v79, v160, s[30:31]
	v_cndmask_b32_e64 v78, v78, v160, s[28:29]
	v_cndmask_b32_e64 v77, v77, v160, s[26:27]
	v_cndmask_b32_e64 v76, v76, v160, s[24:25]
	v_cndmask_b32_e64 v75, v75, v160, s[22:23]
	v_cndmask_b32_e64 v74, v74, v160, s[20:21]
	v_cndmask_b32_e64 v73, v73, v160, s[18:19]
	v_cndmask_b32_e64 v72, v72, v160, s[16:17]
	v_cndmask_b32_e64 v71, v71, v160, s[14:15]
	v_cndmask_b32_e64 v70, v70, v160, s[12:13]
	v_cndmask_b32_e64 v69, v69, v160, s[10:11]
	v_cndmask_b32_e64 v68, v68, v160, s[8:9]
	v_cndmask_b32_e64 v67, v67, v160, s[6:7]
	v_cndmask_b32_e32 v66, v66, v160, vcc
.LBB0_271:
	v_max_f32_e32 v122, v82, v83
	v_max3_f32 v122, v122, v84, v85
	v_max3_f32 v122, v122, v86, v87
	v_max3_f32 v122, v122, v88, v89
	v_max3_f32 v122, v122, v90, v91
	v_max3_f32 v122, v122, v92, v93
	v_max3_f32 v122, v122, v94, v95
	v_max3_f32 v122, v122, v96, v97
	v_max3_f32 v122, v122, v66, v67
	v_max3_f32 v122, v122, v68, v69
	v_max3_f32 v122, v122, v70, v71
	v_max3_f32 v122, v122, v72, v73
	v_max3_f32 v122, v122, v74, v75
	v_max3_f32 v122, v122, v76, v77
	v_max3_f32 v122, v122, v78, v79
	v_max3_f32 v122, v122, v80, v81
	v_mov_b32_e32 v123, v122
	s_nop 1
	v_permlane32_swap_b32_e32 v122, v123
	v_max_f32_e32 v122, v122, v123
	v_sub_f32_e32 v123, v122, v121
	v_mul_f32_e32 v123, 0x3e000000, v123
	v_cmp_ge_f32_e32 vcc, s33, v123
	v_max_f32_e32 v122, v121, v122
	v_sub_f32_e32 v123, v121, v122
	v_mul_f32_e32 v123, 0x3e38aa3b, v123
	s_cmp_eq_u64 vcc, exec
	v_exp_f32_e32 v123, v123
	s_cselect_b64 vcc, -1, 0
	v_cndmask_b32_e32 v139, v122, v121, vcc
	v_mul_f32_e32 v154, 0xbe38aa3b, v139
	v_fma_f32 v96, v96, s84, v154
	v_fma_f32 v97, v97, s84, v154
	v_fma_f32 v94, v94, s84, v154
	v_fma_f32 v95, v95, s84, v154
	v_fma_f32 v92, v92, s84, v154
	v_fma_f32 v93, v93, s84, v154
	v_fma_f32 v90, v90, s84, v154
	v_fma_f32 v91, v91, s84, v154
	v_fma_f32 v88, v88, s84, v154
	v_fma_f32 v89, v89, s84, v154
	v_fma_f32 v86, v86, s84, v154
	v_fma_f32 v87, v87, s84, v154
	v_fma_f32 v84, v84, s84, v154
	v_fma_f32 v85, v85, s84, v154
	v_fma_f32 v82, v82, s84, v154
	v_fma_f32 v83, v83, s84, v154
	v_cndmask_b32_e64 v121, v123, 1.0, vcc
	v_exp_f32_e32 v136, v82
	v_exp_f32_e32 v137, v83
	v_exp_f32_e32 v134, v84
	v_exp_f32_e32 v135, v85
	v_exp_f32_e32 v132, v86
	v_exp_f32_e32 v133, v87
	v_exp_f32_e32 v130, v88
	v_exp_f32_e32 v131, v89
	v_exp_f32_e32 v128, v90
	v_exp_f32_e32 v129, v91
	v_exp_f32_e32 v126, v92
	v_exp_f32_e32 v127, v93
	v_exp_f32_e32 v124, v94
	v_exp_f32_e32 v125, v95
	v_exp_f32_e32 v122, v96
	v_exp_f32_e32 v123, v97
	v_cmp_gt_f32_e32 vcc, 1.0, v121
	s_cbranch_vccz .LBB0_275
	s_and_saveexec_b64 s[6:7], s[4:5]
	ds_write_b32 v182, v121 offset:128
	s_or_b64 exec, exec, s[6:7]
	s_waitcnt lgkmcnt(0)
	ds_read_b128 v[82:85], v179 offset:224
	ds_read_b128 v[86:89], v179 offset:192
	ds_read_b128 v[90:93], v179 offset:160
	ds_read_b128 v[94:97], v179 offset:128
	s_waitcnt lgkmcnt(3)
	v_pk_mul_f32 v[32:33], v[32:33], v[84:85]
	s_waitcnt lgkmcnt(2)
	v_pk_mul_f32 v[28:29], v[28:29], v[88:89]
	s_waitcnt lgkmcnt(1)
	v_pk_mul_f32 v[24:25], v[24:25], v[92:93]
	s_waitcnt lgkmcnt(0)
	v_pk_mul_f32 v[20:21], v[20:21], v[96:97]
	v_pk_mul_f32 v[30:31], v[30:31], v[82:83]
	v_pk_mul_f32 v[26:27], v[26:27], v[86:87]
	v_pk_mul_f32 v[22:23], v[22:23], v[90:91]
	v_pk_mul_f32 v[18:19], v[18:19], v[94:95]
	v_pk_mul_f32 v[48:49], v[48:49], v[84:85]
	v_pk_mul_f32 v[44:45], v[44:45], v[88:89]
	v_pk_mul_f32 v[40:41], v[40:41], v[92:93]
	v_pk_mul_f32 v[36:37], v[36:37], v[96:97]
	v_pk_mul_f32 v[46:47], v[46:47], v[82:83]
	v_pk_mul_f32 v[42:43], v[42:43], v[86:87]
	v_pk_mul_f32 v[38:39], v[38:39], v[90:91]
	v_pk_mul_f32 v[34:35], v[34:35], v[94:95]
	v_pk_mul_f32 v[64:65], v[64:65], v[84:85]
	v_pk_mul_f32 v[60:61], v[60:61], v[88:89]
	v_pk_mul_f32 v[56:57], v[56:57], v[92:93]
	v_pk_mul_f32 v[52:53], v[52:53], v[96:97]
	v_pk_mul_f32 v[62:63], v[62:63], v[82:83]
	v_pk_mul_f32 v[58:59], v[58:59], v[86:87]
	v_pk_mul_f32 v[54:55], v[54:55], v[90:91]
	v_pk_mul_f32 v[50:51], v[50:51], v[94:95]
	v_pk_mul_f32 v[16:17], v[16:17], v[84:85]
	v_pk_mul_f32 v[12:13], v[12:13], v[88:89]
	v_pk_mul_f32 v[8:9], v[8:9], v[92:93]
	v_pk_mul_f32 v[4:5], v[4:5], v[96:97]
	v_pk_mul_f32 v[14:15], v[14:15], v[82:83]
	v_pk_mul_f32 v[10:11], v[10:11], v[86:87]
	v_pk_mul_f32 v[6:7], v[6:7], v[90:91]
	v_pk_mul_f32 v[2:3], v[2:3], v[94:95]
.LBB0_275:
	v_mov_b32_e32 v155, v154
	v_mov_b32_e32 v82, v154
	v_mov_b32_e32 v83, v154
	v_fma_f32 v154, v66, s84, v154
	v_fma_f32 v155, v67, s84, v155
	v_add_f32_e32 v66, v114, v115
	v_fmac_f32_e32 v66, v181, v180
	v_add_f32_e32 v67, v116, v117
	s_addk_i32 s95, 0x100
	v_fmac_f32_e32 v67, v66, v184
	v_add_f32_e32 v66, v120, v186
	s_waitcnt vmcnt(0)
	s_add_u32 s70, s70, 0x100000
	v_fmac_f32_e32 v66, v67, v185
	v_add_f32_e32 v180, v138, v195
	s_addc_u32 s71, s71, 0
	s_add_i32 s75, s75, 4
	v_fma_f32 v140, v80, s84, v82
	v_fma_f32 v141, v81, s84, v83
	v_fma_f32 v142, v78, s84, v82
	v_fma_f32 v143, v79, s84, v83
	v_fma_f32 v144, v76, s84, v82
	v_fma_f32 v145, v77, s84, v83
	v_fma_f32 v146, v74, s84, v82
	v_fma_f32 v147, v75, s84, v83
	v_fma_f32 v148, v72, s84, v82
	v_fma_f32 v149, v73, s84, v83
	v_fma_f32 v150, v70, s84, v82
	v_fma_f32 v151, v71, s84, v83
	v_fma_f32 v152, v68, s84, v82
	v_fma_f32 v153, v69, s84, v83
	v_fmac_f32_e32 v180, v66, v187
	s_cmp_ge_u32 s75, s94
	v_add_u32_e32 v183, 0xffffff00, v183
	s_barrier
	s_cbranch_scc1 .LBB0_278
	v_mov_b32_e32 v181, v121
	s_branch .LBB0_251
